# retention output phase: eight just-in-time operand loads at the head of the task body hoisted into free VGPRs and issued with the first batch (counted waits recomputed)
# speedup vs baseline: 1.0088x; 1.0088x over previous
; __device__ __forceinline__ f32x4 mfma16(bf16x8 a, bf16x8 b, f32x4 c) { return __builtin_amdgcn_mfma_f32_16x16x32_bf16(a, b, c, 0, 0, 0); }
; __device__ __forceinline__ void ret_task(const Frame& F, int l, int task) {
;     ...
;     bf16x8 Qf[2][4], Kf[2][2][4];
; #pragma unroll
;     for (int qb = 0; qb < 2; ++qb)
; #pragma unroll
;         for (int ks = 0; ks < 4; ++ks) Qf[qb][ks] = ld_b8(TOK + (size_t)(tq0 + qb * 16 + c) * TOKP + TK_QR + h * HD + ks * 32 + rq * 8);
; #pragma unroll
;     for (int g = 0; g < 2; ++g)
; #pragma unroll
;         for (int ab = 0; ab < 2; ++ab) { const int key = 32 * g + (c >> 2) * 8 + 4 * ab + (c & 3);
; #pragma unroll
;             for (int ks = 0; ks < 4; ++ks) Kf[g][ab][ks] = ld_b8(TOK + (size_t)(tc0 + key) * TOKP + TK_KR + h * HD + rq * 8 + ks * 32); }
;     f32x4 acc[2][8];
; #pragma unroll
;     for (int qb = 0; qb < 2; ++qb)
; #pragma unroll
;         for (int eb = 0; eb < 8; ++eb) acc[qb][eb] = (f32x4){0.f, 0.f, 0.f, 0.f};
;     const bf16* sp = ST + (((size_t)bhh * NCH + n) * HD + c) * HD + rq * 8;
; #pragma unroll
;     for (int eb = 0; eb < 8; ++eb)
; #pragma unroll
;         for (int ks = 0; ks < 4; ++ks) { const bf16x8 sf = ld_b8(sp + eb * 16 * HD + ks * 32);
; #pragma unroll
;             for (int qb = 0; qb < 2; ++qb) acc[qb][eb] = mfma16(sf, Qf[qb][ks], acc[qb][eb]); }
.LBB0_655:
	s_bfe_u32 s1, s8, 0x50001
	s_ashr_i32 s0, s8, 9
	s_lshl_b32 s4, s0, 3
	s_lshl_b32 s0, s0, 11
	s_lshl_b32 s5, s1, 6
	v_and_b32_e32 v180, 15, v118
	s_or_b32 s0, s5, s0
	v_readlane_b32 s5, v251, 32
	v_ashrrev_i32_e32 v205, 4, v118
	s_or_b32 s4, s4, s9
	v_or_b32_e32 v209, s5, v180
	v_or_b32_e32 v196, s0, v209
	v_lshlrev_b32_e32 v202, 3, v205
	v_mov_b64_e32 v[160:161], s[80:81]
	s_movk_i32 s7, 0x2900
	s_ashr_i32 s5, s4, 31
	v_ashrrev_i32_e32 v203, 31, v202
	v_mad_i64_i32 v[198:199], s[12:13], v196, s7, v[160:161]
	s_lshl_b32 s96, s9, 8
	s_lshl_b64 s[4:5], s[4:5], 12
	s_lshl_b32 s1, s1, 7
	s_waitcnt lgkmcnt(0)
	v_lshl_add_u64 v[0:1], v[198:199], 0, s[96:97]
	v_lshlrev_b64 v[176:177], 1, v[202:203]
	s_or_b32 s1, s4, s1
	v_lshl_add_u64 v[8:9], v[0:1], 0, v[176:177]
	v_mov_b32_e32 v0, s1
	v_mov_b32_e32 v1, s5
	v_readlane_b32 s4, v253, 46
	v_lshlrev_b64 v[0:1], 8, v[0:1]
	v_readlane_b32 s5, v253, 47
	v_or_b32_e32 v194, 16, v196
	s_movk_i32 s6, 0x1000
	v_lshl_add_u64 v[0:1], s[4:5], 0, v[0:1]
	v_mad_i64_i32 v[200:201], s[4:5], v194, s7, v[160:161]
	v_add_co_u32_e32 v4, vcc, s6, v8
	s_mov_b64 s[4:5], 0x1000
	v_lshlrev_b32_e32 v2, 4, v180
	v_lshl_or_b32 v2, v205, 8, v2
	v_mov_b32_e32 v3, 0
	v_lshl_add_u64 v[36:37], v[0:1], 0, v[2:3]
	v_addc_co_u32_e32 v5, vcc, 0, v9, vcc
	v_lshl_add_u64 v[8:9], v[8:9], 0, s[4:5]
	global_load_dwordx4 v[0:3], v[36:37], off
	global_load_dwordx4 v[46:49], v[36:37], off offset:1024
	v_and_b32_e32 v242, -16, v196
	v_lshlrev_b32_e32 v242, 12, v242
	v_lshl_add_u32 v242, v180, 4, v242
	v_lshl_add_u32 v242, v205, 8, v242
	s_lshl_b32 s100, s9, 12
	v_add_u32_e32 v242, s100, v242
	v_add_u32_e32 v242, 0xe000000, v242
	v_mov_b32_e32 v243, 0
	v_mov_b32_e32 v238, s62
	v_mov_b32_e32 v239, s63
	v_lshl_add_u64 v[238:239], v[238:239], 0, v[242:243]
	v_mov_b32_e32 v242, 0x10000
	v_lshl_add_u64 v[240:241], v[238:239], 0, v[242:243]
	v_and_b32_e32 v242, -16, v196
	v_lshlrev_b32_e32 v242, 11, v242
	v_lshl_add_u32 v242, v180, 4, v242
	v_lshrrev_b32_e32 v243, 1, v205
	v_lshl_add_u32 v242, v243, 8, v242
	v_and_b32_e32 v243, 1, v205
	v_lshl_add_u32 v242, v243, 3, v242
	v_add_u32_e32 v242, s100, v242
	v_add_u32_e32 v242, 0x2ec00000, v242
	v_mov_b32_e32 v243, 0
	v_mov_b32_e32 v248, s62
	v_mov_b32_e32 v249, s63
	v_lshl_add_u64 v[248:249], v[248:249], 0, v[242:243]
	global_load_dwordx4 v[20:23], v[238:239], off
	global_load_dwordx4 v[52:55], v[238:239], off offset:1024
	v_lshl_add_u64 v[4:5], v[200:201], 0, s[96:97]
	v_lshl_add_u64 v[12:13], v[4:5], 0, v[176:177]
	v_add_co_u32_e32 v4, vcc, s6, v12
	v_lshl_add_u64 v[80:81], v[12:13], 0, s[4:5]
	s_nop 0
	v_addc_co_u32_e32 v5, vcc, 0, v13, vcc
	global_load_dwordx4 v[24:27], v[240:241], off
	global_load_dwordx4 v[60:63], v[238:239], off offset:2048
	global_load_dwordx4 v[56:59], v[240:241], off offset:1024
	global_load_dwordx4 v[64:67], v[240:241], off offset:2048
	s_movk_i32 s1, 0x2000
	v_add_co_u32_e32 v10, vcc, s1, v36
	s_movk_i32 s1, 0x4000
	s_nop 0
	v_addc_co_u32_e32 v11, vcc, 0, v37, vcc
	s_waitcnt lgkmcnt(0)
	global_load_dwordx4 v[14:17], v[10:11], off offset:-4096
	global_load_dwordx4 v[72:75], v[238:239], off offset:3072
	s_waitcnt vmcnt(19)
	v_add_co_u32_e32 v50, vcc, s1, v36
	global_load_dwordx4 v[28:31], v[10:11], off
	s_nop 0
	v_addc_co_u32_e32 v51, vcc, 0, v37, vcc
	v_add_co_u32_e32 v84, vcc, s6, v36
	global_load_dwordx4 v[38:41], v[50:51], off offset:-4096
	global_load_dwordx4 v[112:115], v[50:51], off offset:2048
	v_addc_co_u32_e32 v85, vcc, 0, v37, vcc
	global_load_dwordx4 v[120:123], v[84:85], off offset:1024
	global_load_dwordx4 v[124:127], v[10:11], off offset:1024
	global_load_dwordx4 v[128:131], v[36:37], off offset:2048
	global_load_dwordx4 v[132:135], v[84:85], off offset:2048
	global_load_dwordx4 v[136:139], v[36:37], off offset:3072
	global_load_dwordx4 v[140:143], v[10:11], off offset:2048
	global_load_dwordx4 v[144:147], v[10:11], off offset:3072
	global_load_dwordx4 v[148:151], v[84:85], off offset:3072
	s_movk_i32 s1, 0x3000
	v_lshlrev_b32_e32 v119, 1, v118
	v_and_b32_e32 v118, 3, v118
	s_mov_b64 s[10:11], 0x1800
	s_lshl_b32 s9, s9, 7
	v_or_b32_e32 v228, 16, v209
	v_mov_b32_e32 v210, v202
	v_mov_b32_e32 v195, v202
	s_waitcnt vmcnt(18)
	v_mfma_f32_16x16x32_bf16 v[4:7], v[0:3], v[20:23], 0
	global_load_dwordx4 v[80:83], v[240:241], off offset:3072
	s_waitcnt vmcnt(17)
	v_mfma_f32_16x16x32_bf16 v[0:3], v[0:3], v[24:27], 0
	v_mfma_f32_16x16x32_bf16 v[4:7], v[46:49], v[52:55], v[4:7]
	s_waitcnt vmcnt(15)
	v_mfma_f32_16x16x32_bf16 v[0:3], v[46:49], v[56:59], v[0:3]
	s_waitcnt vmcnt(13)
	v_mfma_f32_16x16x32_bf16 v[32:35], v[14:17], v[20:23], 0
	v_mfma_f32_16x16x32_bf16 v[14:17], v[14:17], v[24:27], 0
	s_waitcnt vmcnt(10)
	v_mfma_f32_16x16x32_bf16 v[68:71], v[38:41], v[20:23], 0
	s_waitcnt vmcnt(0)
	v_mfma_f32_16x16x32_bf16 v[12:15], v[120:123], v[56:59], v[14:17]
	s_nop 3
	v_mfma_f32_16x16x32_bf16 v[42:45], v[28:31], v[20:23], 0
	v_mfma_f32_16x16x32_bf16 v[28:31], v[28:31], v[24:27], 0
	v_mfma_f32_16x16x32_bf16 v[32:35], v[120:123], v[52:55], v[32:35]
	s_waitcnt vmcnt(0)
	v_mfma_f32_16x16x32_bf16 v[42:45], v[124:127], v[52:55], v[42:45]
	v_mfma_f32_16x16x32_bf16 v[16:19], v[124:127], v[56:59], v[28:31]
	s_nop 2
	s_waitcnt vmcnt(0)
	v_mfma_f32_16x16x32_bf16 v[76:79], v[132:135], v[64:67], v[12:15]
	s_nop 2
	v_mfma_f32_16x16x32_bf16 v[4:7], v[128:131], v[60:63], v[4:7]
	v_mfma_f32_16x16x32_bf16 v[0:3], v[128:131], v[64:67], v[0:3]
	v_mfma_f32_16x16x32_bf16 v[46:49], v[132:135], v[60:63], v[32:35]
	s_nop 2
	s_waitcnt vmcnt(0)
	v_mfma_f32_16x16x32_bf16 v[28:31], v[136:139], v[80:83], v[0:3]
	s_nop 2
	s_waitcnt vmcnt(0)
; __device__ __forceinline__ f32x4 mfma16(bf16x8 a, bf16x8 b, f32x4 c) { return __builtin_amdgcn_mfma_f32_16x16x32_bf16(a, b, c, 0, 0, 0); }
; __device__ __forceinline__ void ret_task(const Frame& F, int l, int task) {
;     ...
;     const bf16* sp = ST + (((size_t)bhh * NCH + n) * HD + c) * HD + rq * 8;
; #pragma unroll
;     for (int eb = 0; eb < 8; ++eb)
; #pragma unroll
;         for (int ks = 0; ks < 4; ++ks) { const bf16x8 sf = ld_b8(sp + eb * 16 * HD + ks * 32);
; #pragma unroll
;             for (int qb = 0; qb < 2; ++qb) acc[qb][eb] = mfma16(sf, Qf[qb][ks], acc[qb][eb]); }
;     bf16x8 Vf[8];
; #pragma unroll
;     for (int eb = 0; eb < 8; ++eb) Vf[eb] = ld_b8(SWP + (size_t)(SW_VR + h * HD + eb * 16 + c) * SWPP + tc0 + 8 * rq);
	v_mfma_f32_16x16x32_bf16 v[42:45], v[140:143], v[60:63], v[42:45]
	v_mfma_f32_16x16x32_bf16 v[16:19], v[140:143], v[64:67], v[16:19]
	v_mfma_f32_16x16x32_bf16 v[32:35], v[136:139], v[72:75], v[4:7]
	s_nop 2
	v_add_co_u32_e32 v84, vcc, s1, v36
	s_movk_i32 s1, 0x6000
	s_nop 0
	v_addc_co_u32_e32 v85, vcc, 0, v37, vcc
	s_waitcnt vmcnt(0)
	v_mfma_f32_16x16x32_bf16 v[12:15], v[148:151], v[72:75], v[46:49]
	s_nop 2
	global_load_dwordx4 v[46:49], v[84:85], off offset:1024
	v_add_co_u32_e32 v116, vcc, s1, v36
	v_mfma_f32_16x16x32_bf16 v[8:11], v[148:151], v[80:83], v[76:79]
	s_nop 0
	v_addc_co_u32_e32 v117, vcc, 0, v37, vcc
	s_movk_i32 s1, 0x5000
	v_mfma_f32_16x16x32_bf16 v[4:7], v[144:147], v[72:75], v[42:45]
	global_load_dwordx4 v[76:79], v[84:85], off offset:3072
	global_load_dwordx4 v[92:95], v[116:117], off
	global_load_dwordx4 v[88:91], v[116:117], off offset:1024
	global_load_dwordx4 v[42:45], v[84:85], off offset:2048
	v_mfma_f32_16x16x32_bf16 v[0:3], v[144:147], v[80:83], v[16:19]
	global_load_dwordx4 v[108:111], v[116:117], off offset:-4096
	v_mfma_f32_16x16x32_bf16 v[16:19], v[38:41], v[24:27], 0
	s_waitcnt vmcnt(5)
	v_mfma_f32_16x16x32_bf16 v[38:41], v[46:49], v[52:55], v[68:71]
	s_nop 2
	global_load_dwordx4 v[68:71], v[50:51], off offset:1024
	global_load_dwordx4 v[84:87], v[50:51], off
	v_mfma_f32_16x16x32_bf16 v[16:19], v[46:49], v[56:59], v[16:19]
	s_waitcnt vmcnt(3)
	v_mfma_f32_16x16x32_bf16 v[38:41], v[42:45], v[60:63], v[38:41]
	v_mfma_f32_16x16x32_bf16 v[42:45], v[42:45], v[64:67], v[16:19]
	v_mfma_f32_16x16x32_bf16 v[16:19], v[76:79], v[72:75], v[38:41]
	s_nop 5
	v_add_co_u32_e32 v38, vcc, s1, v36
	v_mfma_f32_16x16x32_bf16 v[40:43], v[76:79], v[80:83], v[42:45]
	s_nop 0
	v_addc_co_u32_e32 v39, vcc, 0, v37, vcc
	global_load_dwordx4 v[96:99], v[38:39], off offset:3072
	global_load_dwordx4 v[104:107], v[38:39], off offset:1024
	global_load_dwordx4 v[100:103], v[38:39], off offset:2048
	s_waitcnt vmcnt(3)
	v_mfma_f32_16x16x32_bf16 v[44:47], v[84:87], v[20:23], 0
	global_load_dwordx4 v[48:51], v[50:51], off offset:3072
	s_movk_i32 s1, 0x7000
	v_mfma_f32_16x16x32_bf16 v[76:79], v[84:87], v[24:27], 0
	v_mfma_f32_16x16x32_bf16 v[44:47], v[68:71], v[52:55], v[44:47]
	v_mfma_f32_16x16x32_bf16 v[68:71], v[68:71], v[56:59], v[76:79]
	s_nop 5
	global_load_dwordx4 v[76:79], v[116:117], off offset:2048
	global_load_dwordx4 v[84:87], v[116:117], off offset:3072
	v_add_co_u32_e32 v116, vcc, s1, v36
	v_mfma_f32_16x16x32_bf16 v[44:47], v[112:115], v[60:63], v[44:47]
	s_nop 0
	v_addc_co_u32_e32 v117, vcc, 0, v37, vcc
	global_load_dwordx4 v[36:39], v[116:117], off offset:1024
	v_mfma_f32_16x16x32_bf16 v[112:115], v[112:115], v[64:67], v[68:71]
	s_ashr_i32 s1, s0, 31
	s_nop 1
	global_load_dwordx4 v[68:71], v[116:117], off
	s_waitcnt vmcnt(4)
	v_mfma_f32_16x16x32_bf16 v[44:47], v[48:51], v[72:75], v[44:47]
	v_mfma_f32_16x16x32_bf16 v[48:51], v[48:51], v[80:83], v[112:115]
	s_nop 2
	v_and_b32_e32 v112, 24, v119
	v_mfma_f32_16x16x32_bf16 v[120:123], v[108:111], v[20:23], 0
	v_or3_b32 v162, v118, v112, s0
	v_and_b32_e32 v242, -16, v162
	v_lshlrev_b32_e32 v242, 12, v242
	v_and_b32_e32 v243, 15, v162
	v_lshl_add_u32 v242, v243, 4, v242
	v_lshl_add_u32 v242, v205, 8, v242
	s_lshl_b32 s100, s9, 5
	s_add_i32 s100, s100, 0x8000
	v_add_u32_e32 v242, s100, v242
	v_add_u32_e32 v242, 0xe000000, v242
	v_mov_b32_e32 v243, 0
	v_mov_b32_e32 v244, s62
	v_mov_b32_e32 v245, s63
	v_lshl_add_u64 v[244:245], v[244:245], 0, v[242:243]
	v_mov_b32_e32 v242, 0x20000
	v_lshl_add_u64 v[246:247], v[244:245], 0, v[242:243]
	v_mad_i64_i32 v[118:119], s[4:5], v162, s7, v[160:161]
	v_mfma_f32_16x16x32_bf16 v[124:127], v[108:111], v[24:27], 0
	global_load_dwordx4 v[112:115], v[116:117], off offset:2048
	v_lshl_add_u64 v[118:119], v[118:119], 0, s[96:97]
	v_lshl_add_u64 v[128:129], v[118:119], 0, v[176:177]
	v_mfma_f32_16x16x32_bf16 v[120:123], v[104:107], v[52:55], v[120:123]
	v_add_co_u32_e32 v108, vcc, s6, v128
	v_mfma_f32_16x16x32_bf16 v[104:107], v[104:107], v[56:59], v[124:127]
	s_nop 0
	v_addc_co_u32_e32 v109, vcc, 0, v129, vcc
	v_lshl_add_u64 v[128:129], v[128:129], 0, s[10:11]
	v_or_b32_e32 v124, 4, v162
	v_mad_i64_i32 v[124:125], s[4:5], v124, s7, v[160:161]
	v_lshl_add_u64 v[124:125], v[124:125], 0, s[96:97]
	global_load_dwordx4 v[108:111], v[244:245], off
	v_lshl_add_u64 v[130:131], v[124:125], 0, v[176:177]
	global_load_dwordx4 v[124:127], v[244:245], off offset:1024
	v_mfma_f32_16x16x32_bf16 v[120:123], v[100:103], v[60:63], v[120:123]
	global_load_dwordx4 v[116:119], v[116:117], off offset:3072
	v_mfma_f32_16x16x32_bf16 v[100:103], v[100:103], v[64:67], v[104:107]
	s_nop 2
	v_add_co_u32_e32 v104, vcc, s6, v130
	v_mfma_f32_16x16x32_bf16 v[144:147], v[96:99], v[72:75], v[120:123]
	s_nop 0
	v_addc_co_u32_e32 v105, vcc, 0, v131, vcc
	v_or_b32_e32 v106, s9, v180
	global_load_dwordx4 v[120:123], v[244:245], off offset:64
	v_mfma_f32_16x16x32_bf16 v[148:151], v[96:99], v[80:83], v[100:103]
	global_load_dwordx4 v[168:171], v[244:245], off offset:2048
	global_load_dwordx4 v[96:99], v[244:245], off offset:3072
	v_mul_u32_u24_e32 v106, 0x4080, v106
	v_lshlrev_b32_e32 v184, 1, v106
	v_mfma_f32_16x16x32_bf16 v[100:103], v[92:95], v[20:23], 0
	v_or_b32_e32 v104, 32, v162
	v_lshl_add_u64 v[106:107], s[64:65], 0, v[184:185]
	v_mad_i64_i32 v[104:105], s[4:5], v104, s7, v[160:161]
	v_mfma_f32_16x16x32_bf16 v[92:95], v[92:95], v[24:27], 0
	v_lshl_add_u64 v[106:107], s[0:1], 1, v[106:107]
	v_lshl_add_u64 v[178:179], v[106:107], 0, v[176:177]
	v_lshlrev_b32_e32 v242, 4, v180
	v_lshl_add_u32 v242, v205, 8, v242
	v_lshl_add_u32 v242, s9, 15, v242
	v_lshl_add_u32 v242, s0, 5, v242
	v_add_u32_e32 v242, 0x30c00000, v242
	v_mov_b32_e32 v243, 0
	v_mov_b32_e32 v238, s62
	v_mov_b32_e32 v239, s63
	v_lshl_add_u64 v[238:239], v[238:239], 0, v[242:243]
	v_mov_b32_e32 v178, v238
	v_mov_b32_e32 v179, v239
	s_mov_b32 s4, 0x380000
	v_mfma_f32_16x16x32_bf16 v[100:103], v[88:91], v[52:55], v[100:103]
	v_add_co_u32_e32 v106, vcc, s4, v178
	v_lshl_add_u64 v[128:129], v[130:131], 0, s[10:11]
	v_mfma_f32_16x16x32_bf16 v[88:91], v[88:91], v[56:59], v[92:95]
	v_addc_co_u32_e32 v107, vcc, 0, v179, vcc
	s_waitcnt vmcnt(10)
; __device__ __forceinline__ f32x4 mfma16(bf16x8 a, bf16x8 b, f32x4 c) { return __builtin_amdgcn_mfma_f32_16x16x32_bf16(a, b, c, 0, 0, 0); }
; __device__ __forceinline__ float fexp2(float x) { return __builtin_amdgcn_exp2f(x); }
; __device__ __forceinline__ void ret_task(const Frame& F, int l, int task) {
;     ...
;     bf16x8 Vf[8];
; #pragma unroll
;     for (int eb = 0; eb < 8; ++eb) Vf[eb] = ld_b8(SWP + (size_t)(SW_VR + h * HD + eb * 16 + c) * SWPP + tc0 + 8 * rq);
; #pragma unroll
;     for (int qb = 0; qb < 2; ++qb) { const float f = fexp2((float)(qb2 * 32 + qb * 16 + c + 1) * lg);
; #pragma unroll
;         for (int eb = 0; eb < 8; ++eb) acc[qb][eb] *= f; }
;     f32x4 g4[8]; u32x2 gwq[2][8];
; #pragma unroll
;     for (int g = 0; g < 2; ++g) {
;         if (g <= qb2) {
;             f32x4 sa[2][2];
; #pragma unroll
;             for (int qb = 0; qb < 2; ++qb)
; #pragma unroll
;                 for (int ab = 0; ab < 2; ++ab) sa[qb][ab] = (f32x4){0.f, 0.f, 0.f, 0.f};
; #pragma unroll
;             for (int ab = 0; ab < 2; ++ab)
; #pragma unroll
;                 for (int ks = 0; ks < 4; ++ks)
; #pragma unroll
;                     for (int qb = 0; qb < 2; ++qb) sa[qb][ab] = mfma16(Kf[g][ab][ks], Qf[qb][ks], sa[qb][ab]);
;             bf16x8 Pf[2];
; #pragma unroll
;             for (int qb = 0; qb < 2; ++qb) {
;                 const int i = qb2 * 32 + qb * 16 + c;
; #pragma unroll
;                 for (int ab = 0; ab < 2; ++ab)
; #pragma unroll
;                     for (int e = 0; e < 4; ++e) { const int diff = i - (32 * g + 8 * rq + 4 * ab + e);
;                         sa[qb][ab][e] = diff >= 0 ? sa[qb][ab][e] * fexp2((float)diff * lg) : 0.f; }
	v_mfma_f32_16x16x32_bf16 v[92:95], v[76:79], v[60:63], v[100:103]
	v_mfma_f32_16x16x32_bf16 v[100:103], v[76:79], v[64:67], v[88:91]
	global_load_dwordx4 v[76:79], v[106:107], off
	global_load_dwordx4 v[172:175], v[244:245], off offset:1088
	s_nop 1
	v_lshl_add_u64 v[88:89], v[104:105], 0, s[96:97]
	s_waitcnt vmcnt(11)
	v_mfma_f32_16x16x32_bf16 v[152:155], v[84:87], v[72:75], v[92:95]
	v_lshl_add_u64 v[104:105], v[88:89], 0, v[176:177]
	global_load_dwordx4 v[88:91], v[244:245], off offset:3136
	v_lshl_add_u64 v[106:107], v[104:105], 0, s[10:11]
	v_mfma_f32_16x16x32_bf16 v[156:159], v[84:87], v[80:83], v[100:103]
	global_load_dwordx4 v[84:87], v[244:245], off offset:2112
	v_add_co_u32_e32 v104, vcc, s6, v104
	s_waitcnt vmcnt(11)
	v_mfma_f32_16x16x32_bf16 v[92:95], v[68:71], v[20:23], 0
	v_addc_co_u32_e32 v105, vcc, 0, v105, vcc
	global_load_dwordx4 v[132:135], v[246:247], off offset:1024
	global_load_dwordx4 v[128:131], v[246:247], off offset:2048
	v_mfma_f32_16x16x32_bf16 v[100:103], v[68:71], v[24:27], 0
	v_or_b32_e32 v68, 36, v162
	v_mad_i64_i32 v[68:69], s[4:5], v68, s7, v[160:161]
	v_mfma_f32_16x16x32_bf16 v[92:95], v[36:39], v[52:55], v[92:95]
	s_mov_b32 s4, 0
	v_add_co_u32_e32 v70, vcc, s4, v178
	v_mfma_f32_16x16x32_bf16 v[36:39], v[36:39], v[56:59], v[100:103]
	s_nop 0
	v_addc_co_u32_e32 v71, vcc, 0, v179, vcc
	s_mov_b32 s4, 0x80000
	s_waitcnt vmcnt(12)
	v_mfma_f32_16x16x32_bf16 v[36:39], v[112:115], v[64:67], v[36:39]
	global_load_dwordx4 v[140:143], v[246:247], off
	global_load_dwordx4 v[136:139], v[246:247], off offset:3072
	v_lshl_add_u64 v[68:69], v[68:69], 0, s[96:97]
	v_lshl_add_u64 v[68:69], v[68:69], 0, v[176:177]
	v_mfma_f32_16x16x32_bf16 v[100:103], v[112:115], v[60:63], v[92:95]
	s_nop 2
	global_load_dwordx4 v[92:95], v[70:71], off
	v_add_co_u32_e32 v70, vcc, s4, v178
	s_mov_b32 s4, 0x100000
	s_nop 0
	v_addc_co_u32_e32 v71, vcc, 0, v179, vcc
	v_add_co_u32_e32 v104, vcc, s4, v178
	s_waitcnt vmcnt(12)
	v_mfma_f32_16x16x32_bf16 v[164:167], v[116:119], v[80:83], v[36:39]
	v_addc_co_u32_e32 v105, vcc, 0, v179, vcc
	s_mov_b32 s4, 0x180000
	v_mfma_f32_16x16x32_bf16 v[36:39], v[108:111], v[20:23], 0
	v_mfma_f32_16x16x32_bf16 v[108:111], v[108:111], v[24:27], 0
	v_mfma_f32_16x16x32_bf16 v[160:163], v[116:119], v[72:75], v[100:103]
	s_nop 2
	global_load_dwordx4 v[100:103], v[70:71], off
	s_nop 0
	global_load_dwordx4 v[104:107], v[104:105], off
	v_add_co_u32_e32 v70, vcc, s4, v178
	s_mov_b32 s4, 0x200000
	s_nop 0
	v_addc_co_u32_e32 v71, vcc, 0, v179, vcc
	v_add_co_u32_e32 v116, vcc, s4, v178
	v_readlane_b32 s4, v251, 33
	s_nop 0
	v_addc_co_u32_e32 v117, vcc, 0, v179, vcc
	v_mfma_f32_16x16x32_bf16 v[36:39], v[124:127], v[52:55], v[36:39]
	global_load_dwordx4 v[112:115], v[70:71], off
	s_nop 0
	global_load_dwordx4 v[116:119], v[116:117], off
	v_add_u32_e32 v70, s4, v180
	v_cvt_f32_ubyte0_e32 v71, v70
	v_mfma_f32_16x16x32_bf16 v[108:111], v[124:127], v[56:59], v[108:111]
	v_add_u32_e32 v70, 16, v70
	v_cvt_f32_ubyte0_e32 v70, v70
	v_or_b32_e32 v126, 2, v202
	v_mul_f32_e32 v71, v197, v71
	v_mul_f32_e32 v70, v197, v70
	s_waitcnt vmcnt(14)
	v_mfma_f32_16x16x32_bf16 v[36:39], v[168:171], v[60:63], v[36:39]
	v_exp_f32_e32 v204, v71
	v_exp_f32_e32 v206, v70
	v_or_b32_e32 v127, 3, v202
	v_mfma_f32_16x16x32_bf16 v[108:111], v[168:171], v[64:67], v[108:111]
	v_sub_u32_e32 v169, v209, v202
	v_sub_u32_e32 v170, v209, v126
	v_cvt_f32_u32_e32 v70, v169
	v_cvt_f32_u32_e32 v71, v170
	s_waitcnt vmcnt(13)
	v_mfma_f32_16x16x32_bf16 v[36:39], v[96:99], v[72:75], v[36:39]
	v_or_b32_e32 v168, 1, v202
	v_mul_f32_e32 v70, v197, v70
	v_mul_f32_e32 v71, v197, v71
	v_exp_f32_e32 v70, v70
	v_exp_f32_e32 v71, v71
	v_mfma_f32_16x16x32_bf16 v[96:99], v[96:99], v[80:83], v[108:111]
	s_nop 1
	v_mov_b32_e32 v124, v36
	v_mov_b32_e32 v125, v38
	v_pk_mul_f32 v[70:71], v[70:71], v[124:125]
	v_mfma_f32_16x16x32_bf16 v[108:111], v[120:123], v[20:23], 0
	v_cmp_lt_i32_e32 vcc, -1, v170
	v_sub_u32_e32 v125, v209, v127
	v_cvt_f32_u32_e32 v38, v125
	v_mfma_f32_16x16x32_bf16 v[120:123], v[120:123], v[24:27], 0
	v_cndmask_b32_e32 v124, 0, v71, vcc
	v_sub_u32_e32 v71, v209, v168
	v_cvt_f32_u32_e32 v36, v71
	s_waitcnt vmcnt(11)
	v_mfma_f32_16x16x32_bf16 v[108:111], v[172:175], v[52:55], v[108:111]
	v_cmp_lt_i32_e32 vcc, -1, v169
	v_pk_mul_f32 v[14:15], v[204:205], v[14:15] op_sel_hi:[0,1]
	v_mul_f32_e32 v36, v197, v36
	v_mfma_f32_16x16x32_bf16 v[120:123], v[172:175], v[56:59], v[120:123]
	v_mul_f32_e64 v12, v204, v12
	v_mul_f32_e64 v13, v204, v13
	s_mov_b32 s4, 0x280000
	v_pk_mul_f32 v[6:7], v[204:205], v[6:7] op_sel_hi:[0,1]
	s_waitcnt vmcnt(9)
; __device__ __forceinline__ f32x4 mfma16(bf16x8 a, bf16x8 b, f32x4 c) { return __builtin_amdgcn_mfma_f32_16x16x32_bf16(a, b, c, 0, 0, 0); }
; __device__ __forceinline__ float fexp2(float x) { return __builtin_amdgcn_exp2f(x); }
; __device__ __forceinline__ void ret_task(const Frame& F, int l, int task) {
;     ...
;             bf16x8 Pf[2];
; #pragma unroll
;             for (int qb = 0; qb < 2; ++qb) {
;                 const int i = qb2 * 32 + qb * 16 + c;
; #pragma unroll
;                 for (int ab = 0; ab < 2; ++ab)
; #pragma unroll
;                     for (int e = 0; e < 4; ++e) { const int diff = i - (32 * g + 8 * rq + 4 * ab + e);
;                         sa[qb][ab][e] = diff >= 0 ? sa[qb][ab][e] * fexp2((float)diff * lg) : 0.f; }
;                 Pf[qb] = pack8(sa[qb][0], sa[qb][1]);
;             }
; #pragma unroll
;             for (int eb = 0; eb < 8; ++eb)
; #pragma unroll
;                 for (int qb = 0; qb < 2; ++qb) acc[qb][eb] = mfma16(Vf[eb], Pf[qb], acc[qb][eb]);
	v_mfma_f32_16x16x32_bf16 v[108:111], v[84:87], v[60:63], v[108:111]
	v_mul_f32_e64 v4, v204, v4
	v_mul_f32_e64 v5, v204, v5
	v_pk_mul_f32 v[30:31], v[206:207], v[30:31] op_sel_hi:[0,1]
	v_pk_mul_f32 v[28:29], v[206:207], v[28:29] op_sel_hi:[0,1]
	v_mfma_f32_16x16x32_bf16 v[84:87], v[84:87], v[64:67], v[120:123]
	v_mul_f32_e64 v2, v206, v2
	v_mul_f32_e64 v3, v206, v3
	v_pk_mul_f32 v[0:1], v[206:207], v[0:1] op_sel_hi:[0,1]
	v_pk_mul_f32 v[34:35], v[204:205], v[34:35] op_sel_hi:[0,1]
	v_exp_f32_e32 v120, v36
	v_mul_f32_e32 v36, v197, v38
	v_exp_f32_e32 v121, v36
	v_mov_b32_e32 v38, v37
	v_cndmask_b32_e32 v122, 0, v70, vcc
	v_cmp_lt_i32_e32 vcc, -1, v71
	v_pk_mul_f32 v[36:37], v[120:121], v[38:39]
	v_mfma_f32_16x16x32_bf16 v[108:111], v[88:91], v[72:75], v[108:111]
	v_sub_u32_e32 v39, v228, v126
	v_cvt_f32_u32_e32 v70, v39
	v_sub_u32_e32 v120, v228, v127
	v_mfma_f32_16x16x32_bf16 v[84:87], v[88:91], v[80:83], v[84:87]
	v_cndmask_b32_e32 v88, 0, v36, vcc
	v_cmp_lt_i32_e32 vcc, -1, v125
	v_sub_u32_e32 v91, v228, v168
	v_sub_u32_e32 v89, v228, v202
	v_cndmask_b32_e32 v90, 0, v37, vcc
	v_cvt_f32_u32_e32 v37, v91
	v_cvt_f32_u32_e32 v36, v89
	v_mov_b32_e32 v71, v98
	v_cmp_lt_i32_e32 vcc, -1, v39
	v_mul_f32_e32 v37, v197, v37
	v_mul_f32_e32 v36, v197, v36
	v_exp_f32_e32 v38, v37
	v_mul_f32_e32 v37, v197, v70
	v_exp_f32_e32 v36, v36
	v_exp_f32_e32 v37, v37
	v_mov_b32_e32 v70, v96
	v_cvt_f32_u32_e32 v96, v120
	v_mov_b32_e32 v98, v97
	v_pk_mul_f32 v[36:37], v[36:37], v[70:71]
	v_or_b32_e32 v123, 5, v202
	v_cndmask_b32_e32 v121, 0, v37, vcc
	v_mul_f32_e32 v37, v197, v96
	v_exp_f32_e32 v39, v37
	v_cmp_lt_i32_e32 vcc, -1, v89
	v_or_b32_e32 v97, 6, v202
	v_sub_u32_e32 v125, v209, v123
	v_cndmask_b32_e32 v89, 0, v36, vcc
	v_pk_mul_f32 v[36:37], v[38:39], v[98:99]
	v_cmp_lt_i32_e32 vcc, -1, v91
	v_or_b32_e32 v98, 4, v202
	v_sub_u32_e32 v99, v209, v98
	v_cndmask_b32_e32 v91, 0, v36, vcc
	v_cmp_lt_i32_e32 vcc, -1, v120
	v_sub_u32_e32 v39, v209, v97
	v_cvt_f32_u32_e32 v36, v99
	v_cndmask_b32_e32 v96, 0, v37, vcc
	v_cvt_f32_u32_e32 v37, v125
	v_cvt_f32_u32_e32 v70, v39
	v_or_b32_e32 v120, 7, v202
	v_mul_f32_e32 v36, v197, v36
	v_mul_f32_e32 v37, v197, v37
	v_exp_f32_e32 v38, v37
	v_mul_f32_e32 v37, v197, v70
	v_exp_f32_e32 v36, v36
	v_sub_u32_e32 v126, v209, v120
	v_exp_f32_e32 v37, v37
	v_mov_b32_e32 v70, v108
	v_cvt_f32_u32_e32 v108, v126
	v_mov_b32_e32 v71, v110
	v_pk_mul_f32 v[36:37], v[36:37], v[70:71]
	v_cmp_lt_i32_e32 vcc, -1, v39
	v_mov_b32_e32 v110, v109
	v_sub_u32_e32 v98, v228, v98
	v_cndmask_b32_e32 v127, 0, v37, vcc
	v_mul_f32_e32 v37, v197, v108
	v_exp_f32_e32 v39, v37
	v_cmp_lt_i32_e32 vcc, -1, v99
	v_mov_b32_e32 v71, v86
	v_mov_b32_e32 v86, v85
	v_cndmask_b32_e32 v99, 0, v36, vcc
	v_pk_mul_f32 v[36:37], v[38:39], v[110:111]
	v_cmp_lt_i32_e32 vcc, -1, v125
	v_sub_u32_e32 v39, v228, v97
	v_sub_u32_e32 v97, v228, v123
	v_cndmask_b32_e32 v108, 0, v36, vcc
	v_cmp_lt_i32_e32 vcc, -1, v126
	v_cvt_f32_u32_e32 v36, v98
	v_cvt_f32_u32_e32 v70, v39
	v_cndmask_b32_e32 v109, 0, v37, vcc
	v_cvt_f32_u32_e32 v37, v97
	v_mul_f32_e32 v36, v197, v36
	v_exp_f32_e32 v36, v36
	v_sub_u32_e32 v110, v228, v120
	v_mul_f32_e32 v37, v197, v37
	v_exp_f32_e32 v38, v37
	v_mul_f32_e32 v37, v197, v70
	v_exp_f32_e32 v37, v37
	v_mov_b32_e32 v70, v84
	v_cvt_f32_u32_e32 v84, v110
	v_cmp_lt_i32_e32 vcc, -1, v39
	v_pk_mul_f32 v[36:37], v[36:37], v[70:71]
	s_nop 0
	v_cndmask_b32_e32 v70, 0, v37, vcc
	v_mul_f32_e32 v37, v197, v84
	v_exp_f32_e32 v39, v37
	v_cmp_lt_i32_e32 vcc, -1, v98
	s_nop 1
	v_cndmask_b32_e32 v71, 0, v36, vcc
	v_pk_mul_f32 v[36:37], v[38:39], v[86:87]
	v_bfe_u32 v38, v90, 16, 1
	v_bfe_u32 v39, v88, 16, 1
	v_add3_u32 v39, v88, v39, s76
	v_add3_u32 v38, v90, v38, s76
	s_nop 1
	v_bfe_u32 v88, v122, 16, 1
	v_bfe_u32 v90, v124, 16, 1
	v_cmp_lt_i32_e32 vcc, -1, v97
	v_add3_u32 v90, v124, v90, s76
	v_add3_u32 v88, v122, v88, s76
	s_nop 1
	v_cndmask_b32_e32 v36, 0, v36, vcc
	v_cmp_lt_i32_e32 vcc, -1, v110
	s_nop 2
	v_lshrrev_b32_e32 v88, 16, v88
	v_lshrrev_b32_e32 v90, 16, v90
	v_cndmask_b32_e32 v37, 0, v37, vcc
	v_and_or_b32 v231, v38, s75, v90
	v_and_or_b32 v230, v39, s75, v88
	v_cvt_pk_bf16_f32 v233, v127, v109
	v_cvt_pk_bf16_f32 v232, v99, v108
	v_bfe_u32 v84, v96, 16, 1
	v_bfe_u32 v38, v37, 16, 1
	v_add3_u32 v84, v96, v84, s76
	s_waitcnt vmcnt(3)
	v_mfma_f32_16x16x32_bf16 v[96:99], v[100:103], v[230:233], v[12:15]
	v_bfe_u32 v39, v36, 16, 1
	v_bfe_u32 v85, v91, 16, 1
	v_add3_u32 v37, v37, v38, s76
	v_add_co_u32_e32 v12, vcc, s4, v178
	v_bfe_u32 v38, v89, 16, 1
	s_nop 0
	v_addc_co_u32_e32 v13, vcc, 0, v179, vcc
	s_mov_b32 s4, 0x300000
	v_add3_u32 v85, v91, v85, s76
	v_add3_u32 v36, v36, v39, s76
	v_bfe_u32 v39, v121, 16, 1
	v_add3_u32 v38, v89, v38, s76
	s_waitcnt vmcnt(2)
; __device__ __forceinline__ f32x4 mfma16(bf16x8 a, bf16x8 b, f32x4 c) { return __builtin_amdgcn_mfma_f32_16x16x32_bf16(a, b, c, 0, 0, 0); }
; __device__ __forceinline__ void ret_task(const Frame& F, int l, int task) {
;     ...
; #pragma unroll
;             for (int eb = 0; eb < 8; ++eb)
; #pragma unroll
;                 for (int qb = 0; qb < 2; ++qb) acc[qb][eb] = mfma16(Vf[eb], Pf[qb], acc[qb][eb]);
;         }
;         if (g == 0) {
;             if (qb2) {
; #pragma unroll
;                 for (int eb = 0; eb < 8; ++eb) Vf[eb] = ld_b8(SWP + (size_t)(SW_VR + h * HD + eb * 16 + c) * SWPP + tc0 + 32 + 8 * rq);
;             }
	v_mfma_f32_16x16x32_bf16 v[88:91], v[104:107], v[230:233], v[4:7]
	v_add3_u32 v39, v121, v39, s76
	global_load_dwordx4 v[120:123], v[12:13], off
	v_bfe_u32 v86, v71, 16, 1
	v_add_co_u32_e32 v4, vcc, s4, v178
	v_bfe_u32 v87, v70, 16, 1
	s_nop 0
	v_addc_co_u32_e32 v5, vcc, 0, v179, vcc
	global_load_dwordx4 v[124:127], v[4:5], off
	v_add_co_u32_e32 v6, vcc, s6, v68
	v_lshl_add_u64 v[4:5], v[68:69], 0, s[10:11]
	s_nop 0
	v_addc_co_u32_e32 v7, vcc, 0, v69, vcc
	global_load_dwordx4 v[172:175], v[246:247], off offset:1088
	global_load_dwordx4 v[168:171], v[246:247], off offset:2112
	global_load_dwordx4 v[180:183], v[246:247], off offset:64
	global_load_dwordx4 v[176:179], v[246:247], off offset:3136
	v_add3_u32 v70, v70, v87, s76
	v_add3_u32 v71, v71, v86, s76
	v_lshrrev_b32_e32 v38, 16, v38
	v_lshrrev_b32_e32 v39, 16, v39
	v_lshrrev_b32_e32 v71, 16, v71
	v_lshrrev_b32_e32 v70, 16, v70
	v_and_or_b32 v237, v37, s75, v70
	v_and_or_b32 v236, v36, s75, v71
	v_and_or_b32 v235, v84, s75, v39
	v_and_or_b32 v234, v85, s75, v38
	v_readlane_b32 s4, v251, 34
	v_pk_mul_f32 v[32:33], v[204:205], v[32:33] op_sel_hi:[0,1]
	v_mfma_f32_16x16x32_bf16 v[36:39], v[92:95], v[234:237], v[28:31]
	v_mul_f32_e64 v10, v206, v10
	v_mul_f32_e64 v11, v206, v11
	v_pk_mul_f32 v[8:9], v[206:207], v[8:9] op_sel_hi:[0,1]
	v_pk_mul_f32 v[6:7], v[206:207], v[150:151] op_sel_hi:[0,1]
	v_mfma_f32_16x16x32_bf16 v[28:31], v[104:107], v[234:237], v[0:3]
	v_mul_f32_e64 v4, v206, v148
	v_mul_f32_e64 v5, v206, v149
	v_readlane_b32 s5, v251, 35
	s_andn2_b64 vcc, exec, s[4:5]
	v_pk_mul_f32 v[2:3], v[204:205], v[18:19] op_sel_hi:[0,1]
	v_pk_mul_f32 v[0:1], v[204:205], v[16:17] op_sel_hi:[0,1]
	v_mfma_f32_16x16x32_bf16 v[108:111], v[92:95], v[230:233], v[32:35]
	s_waitcnt vmcnt(7)
	v_mfma_f32_16x16x32_bf16 v[84:87], v[112:115], v[230:233], v[0:3]
	s_nop 2
	v_mul_f32_e64 v2, v206, v42
	v_mul_f32_e64 v3, v206, v43
	v_pk_mul_f32 v[0:1], v[206:207], v[40:41] op_sel_hi:[0,1]
	v_mfma_f32_16x16x32_bf16 v[32:35], v[100:103], v[234:237], v[8:11]
	v_mul_f32_e64 v42, v204, v162
	v_mul_f32_e64 v43, v204, v163
	v_pk_mul_f32 v[40:41], v[204:205], v[160:161] op_sel_hi:[0,1]
	v_mfma_f32_16x16x32_bf16 v[16:19], v[112:115], v[234:237], v[0:3]
	s_nop 2
	v_mul_f32_e64 v2, v204, v46
	v_mul_f32_e64 v3, v204, v47
	v_pk_mul_f32 v[0:1], v[204:205], v[44:45] op_sel_hi:[0,1]
	s_waitcnt vmcnt(5)
	v_mfma_f32_16x16x32_bf16 v[8:11], v[120:123], v[234:237], v[4:7]
	v_mfma_f32_16x16x32_bf16 v[68:71], v[116:119], v[230:233], v[0:3]
	s_nop 2
	v_mul_f32_e64 v2, v206, v50
	v_mul_f32_e64 v3, v206, v51
	v_pk_mul_f32 v[0:1], v[206:207], v[48:49] op_sel_hi:[0,1]
	v_mfma_f32_16x16x32_bf16 v[40:43], v[76:79], v[230:233], v[40:43]
	s_nop 0
	v_mfma_f32_16x16x32_bf16 v[12:15], v[116:119], v[234:237], v[0:3]
	s_nop 2
	v_mul_f32_e64 v2, v204, v146
	v_mul_f32_e64 v3, v204, v147
	v_pk_mul_f32 v[0:1], v[204:205], v[144:145] op_sel_hi:[0,1]
	v_pk_mul_f32 v[146:147], v[206:207], v[166:167] op_sel_hi:[0,1]
	v_pk_mul_f32 v[144:145], v[206:207], v[164:165] op_sel_hi:[0,1]
	v_mfma_f32_16x16x32_bf16 v[48:51], v[120:123], v[230:233], v[0:3]
	s_nop 2
	v_mul_f32_e64 v2, v204, v154
	v_mul_f32_e64 v3, v204, v155
	v_pk_mul_f32 v[0:1], v[204:205], v[152:153] op_sel_hi:[0,1]
	s_waitcnt vmcnt(4)
	s_nop 0
	v_mfma_f32_16x16x32_bf16 v[44:47], v[124:127], v[230:233], v[0:3]
	s_nop 2
	v_mul_f32_e64 v2, v206, v158
	v_mul_f32_e64 v3, v206, v159
	v_pk_mul_f32 v[0:1], v[206:207], v[156:157] op_sel_hi:[0,1]
	s_nop 1
	v_mfma_f32_16x16x32_bf16 v[4:7], v[124:127], v[234:237], v[0:3]
	s_nop 2
	v_cndmask_b32_e64 v0, 0, 1, s[4:5]
	v_cmp_ne_u32_e64 s[34:35], 1, v0
	v_mfma_f32_16x16x32_bf16 v[0:3], v[76:79], v[234:237], v[144:147]
	s_cbranch_vccnz .LBB0_657
	s_lshl_b64 s[0:1], s[0:1], 1
	s_add_u32 s0, s64, s0
	s_addc_u32 s1, s65, s1
	v_lshl_add_u64 v[76:77], s[0:1], 0, v[184:185]
	v_lshl_add_u64 v[76:77], v[202:203], 1, v[76:77]
	v_mov_b32_e32 v76, v238
	v_mov_b32_e32 v77, v239
	v_add_co_u32_e32 v78, vcc, 0, v76
	s_nop 1
	v_addc_co_u32_e32 v79, vcc, 0, v77, vcc
	v_add_co_u32_e32 v100, vcc, 0x80000, v76
	s_nop 1
	v_addc_co_u32_e32 v101, vcc, 0, v77, vcc
	global_load_dwordx4 v[92:95], v[78:79], off offset:1024
	s_nop 0
	global_load_dwordx4 v[100:103], v[100:101], off offset:1024
	v_add_co_u32_e32 v78, vcc, 0x100000, v76
	s_nop 1
	v_addc_co_u32_e32 v79, vcc, 0, v77, vcc
	v_add_co_u32_e32 v112, vcc, 0x180000, v76
	s_nop 1
	v_addc_co_u32_e32 v113, vcc, 0, v77, vcc
	global_load_dwordx4 v[104:107], v[78:79], off offset:1024
	s_nop 0
	global_load_dwordx4 v[112:115], v[112:113], off offset:1024
	v_add_co_u32_e32 v78, vcc, 0x200000, v76
	s_nop 1
	v_addc_co_u32_e32 v79, vcc, 0, v77, vcc
	v_add_co_u32_e32 v120, vcc, 0x280000, v76
	s_nop 1
	v_addc_co_u32_e32 v121, vcc, 0, v77, vcc
	global_load_dwordx4 v[116:119], v[78:79], off offset:1024
	s_nop 0
	global_load_dwordx4 v[120:123], v[120:121], off offset:1024
	v_add_co_u32_e32 v78, vcc, 0x300000, v76
	s_nop 1
	v_addc_co_u32_e32 v79, vcc, 0, v77, vcc
	v_add_co_u32_e32 v76, vcc, 0x380000, v76
	s_nop 1
	v_addc_co_u32_e32 v77, vcc, 0, v77, vcc
	global_load_dwordx4 v[124:127], v[78:79], off offset:1024
	s_nop 0
	global_load_dwordx4 v[76:79], v[76:77], off offset:1024
